# v57 + in-proj K-loop LDS-DMAs use SGPR base + 32-bit lane offset (no per-DMA v_lshl_add_u64, half the address operand)
# speedup vs baseline: 1.0036x; 1.0036x over previous
.LBB0_264:
	s_ashr_i32 s73, s72, 31
	s_lshl_b64 s[26:27], s[72:73], 21
	s_add_u32 s76, s38, s26
	s_addc_u32 s77, s40, s27
	s_and_b64 s[26:27], s[4:5], exec
	s_cselect_b32 s73, s77, s7
	s_cselect_b32 vcc_lo, s76, s6
	s_ashr_i32 s75, s74, 31
	s_lshl_b64 s[26:27], s[74:75], 21
	s_add_u32 s96, s42, s26
	s_addc_u32 s97, s44, s27
	s_and_b64 s[26:27], s[4:5], exec
	s_cselect_b32 s75, s97, s25
	s_cselect_b32 vcc_hi, s96, s24
	s_add_u32 s6, s6, 0x100080
	s_addc_u32 s7, s7, 0
	s_add_u32 s21, s24, 0x100
	s_addc_u32 s13, s25, 0
	s_mov_b32 s58, -2
	s_add_u32 s24, s6, 0xfff00080
	s_addc_u32 s25, s7, -1
	s_add_i32 s28, 0, 0x10000
	s_cmp_eq_u32 s58, 60
	s_cselect_b32 s27, s73, s25
	s_cselect_b32 s26, vcc_lo, s24
	s_cselect_b32 s25, s75, s13
	s_cselect_b32 s24, vcc_hi, s21
	s_add_i32 s71, 0, 0x14000
	v_add_u32_e32 v144, s28, v163
	v_add_u32_e32 v182, s71, v163
	s_waitcnt lgkmcnt(0)
	ds_read_b128 v[132:135], v144
	ds_read_b128 v[136:139], v144 offset:1024
	ds_read_b128 v[140:143], v144 offset:2048
	ds_read_b128 v[144:147], v144 offset:3072
	ds_read_b128 v[148:151], v182
	ds_read_b128 v[152:155], v182 offset:1024
	ds_read_b128 v[178:181], v182 offset:2048
	ds_read_b128 v[186:189], v182 offset:3072
	s_add_i32 m0, s46, 0xc000
	ds_read_b128 v[190:193], v184
	ds_read_b128 v[194:197], v184 offset:1024
	ds_read_b128 v[198:201], v184 offset:2048
	ds_read_b128 v[202:205], v184 offset:3072
	ds_read_b128 v[222:225], v184 offset:4096
	ds_read_b128 v[226:229], v184 offset:5120
	ds_read_b128 v[230:233], v184 offset:6144
	ds_read_b128 v[234:237], v184 offset:7168
	global_load_lds_dwordx4 v174, s[6:7]
	s_add_i32 m0, s46, 0xe000
	s_nop 0
	global_load_lds_dwordx4 v176, s[6:7]
	s_waitcnt vmcnt(8)
	s_waitcnt lgkmcnt(0)
	s_setprio 1
	s_barrier
	v_mfma_f32_16x16x32_bf16 v[120:123], v[132:135], v[190:193], 0
	v_mfma_f32_16x16x32_bf16 v[116:119], v[140:143], v[190:193], 0
	v_mfma_f32_16x16x32_bf16 v[104:107], v[132:135], v[198:201], 0
	v_mfma_f32_16x16x32_bf16 v[100:103], v[140:143], v[198:201], 0
	v_mfma_f32_16x16x32_bf16 v[88:91], v[132:135], v[222:225], 0
	v_mfma_f32_16x16x32_bf16 v[84:87], v[140:143], v[222:225], 0
	v_mfma_f32_16x16x32_bf16 v[72:75], v[132:135], v[230:233], 0
	v_mfma_f32_16x16x32_bf16 v[68:71], v[140:143], v[230:233], 0
	v_mfma_f32_16x16x32_bf16 v[120:123], v[136:139], v[194:197], v[120:123]
	v_mfma_f32_16x16x32_bf16 v[116:119], v[144:147], v[194:197], v[116:119]
	v_mfma_f32_16x16x32_bf16 v[104:107], v[136:139], v[202:205], v[104:107]
	v_mfma_f32_16x16x32_bf16 v[100:103], v[144:147], v[202:205], v[100:103]
	v_mfma_f32_16x16x32_bf16 v[88:91], v[136:139], v[226:229], v[88:91]
	v_mfma_f32_16x16x32_bf16 v[84:87], v[144:147], v[226:229], v[84:87]
	v_mfma_f32_16x16x32_bf16 v[72:75], v[136:139], v[234:237], v[72:75]
	v_mfma_f32_16x16x32_bf16 v[68:71], v[144:147], v[234:237], v[68:71]
	v_mfma_f32_16x16x32_bf16 v[128:131], v[148:151], v[190:193], 0
	v_mfma_f32_16x16x32_bf16 v[124:127], v[178:181], v[190:193], 0
	v_mfma_f32_16x16x32_bf16 v[112:115], v[148:151], v[198:201], 0
	v_mfma_f32_16x16x32_bf16 v[108:111], v[178:181], v[198:201], 0
	v_mfma_f32_16x16x32_bf16 v[96:99], v[148:151], v[222:225], 0
	v_mfma_f32_16x16x32_bf16 v[92:95], v[178:181], v[222:225], 0
	v_mfma_f32_16x16x32_bf16 v[80:83], v[148:151], v[230:233], 0
	v_mfma_f32_16x16x32_bf16 v[76:79], v[178:181], v[230:233], 0
	v_mfma_f32_16x16x32_bf16 v[128:131], v[152:155], v[194:197], v[128:131]
	v_mfma_f32_16x16x32_bf16 v[124:127], v[186:189], v[194:197], v[124:127]
	v_mfma_f32_16x16x32_bf16 v[112:115], v[152:155], v[202:205], v[112:115]
	v_mfma_f32_16x16x32_bf16 v[108:111], v[186:189], v[202:205], v[108:111]
	v_mfma_f32_16x16x32_bf16 v[96:99], v[152:155], v[226:229], v[96:99]
	v_mfma_f32_16x16x32_bf16 v[92:95], v[186:189], v[226:229], v[92:95]
	v_mfma_f32_16x16x32_bf16 v[80:83], v[152:155], v[234:237], v[80:83]
	v_mfma_f32_16x16x32_bf16 v[76:79], v[186:189], v[234:237], v[76:79]
	s_barrier
	s_setprio 0
	s_add_i32 s28, s28, s1
	s_mov_b32 m0, s28
	ds_read_b128 v[190:193], v184 offset:16384
	ds_read_b128 v[194:197], v184 offset:17408
	ds_read_b128 v[198:201], v184 offset:18432
	ds_read_b128 v[202:205], v184 offset:19456
	ds_read_b128 v[222:225], v184 offset:20480
	ds_read_b128 v[226:229], v184 offset:21504
	ds_read_b128 v[230:233], v184 offset:22528
	ds_read_b128 v[234:237], v184 offset:23552
	global_load_lds_dwordx4 v2, s[24:25]
	s_add_i32 m0, s28, 0x2000
	s_add_u32 s28, s24, 0x100000
	s_addc_u32 s29, s25, 0
	s_add_i32 s71, s71, s1
	global_load_lds_dwordx4 v168, s[24:25]
	s_mov_b32 m0, s71
	s_nop 0
	global_load_lds_dwordx4 v2, s[28:29]
	s_add_i32 m0, s71, 0x2000
	s_nop 0
	global_load_lds_dwordx4 v168, s[28:29]
	s_mov_b32 m0, s46
	s_nop 0
	global_load_lds_dwordx4 v172, s[26:27]
	s_mov_b32 m0, s50
	s_nop 0
	global_load_lds_dwordx4 v170, s[26:27]
	s_waitcnt vmcnt(8)
	s_waitcnt lgkmcnt(0)
	s_setprio 1
	s_barrier
	v_mfma_f32_16x16x32_bf16 v[56:59], v[132:135], v[190:193], 0
	v_mfma_f32_16x16x32_bf16 v[52:55], v[140:143], v[190:193], 0
	v_mfma_f32_16x16x32_bf16 v[40:43], v[132:135], v[198:201], 0
	v_mfma_f32_16x16x32_bf16 v[36:39], v[140:143], v[198:201], 0
	v_mfma_f32_16x16x32_bf16 v[24:27], v[132:135], v[222:225], 0
	v_mfma_f32_16x16x32_bf16 v[20:23], v[140:143], v[222:225], 0
	v_mfma_f32_16x16x32_bf16 v[8:11], v[132:135], v[230:233], 0
	v_mfma_f32_16x16x32_bf16 v[4:7], v[140:143], v[230:233], 0
	v_mfma_f32_16x16x32_bf16 v[56:59], v[136:139], v[194:197], v[56:59]
	v_mfma_f32_16x16x32_bf16 v[52:55], v[144:147], v[194:197], v[52:55]
	v_mfma_f32_16x16x32_bf16 v[40:43], v[136:139], v[202:205], v[40:43]
	v_mfma_f32_16x16x32_bf16 v[36:39], v[144:147], v[202:205], v[36:39]
	v_mfma_f32_16x16x32_bf16 v[24:27], v[136:139], v[226:229], v[24:27]
	v_mfma_f32_16x16x32_bf16 v[20:23], v[144:147], v[226:229], v[20:23]
	v_mfma_f32_16x16x32_bf16 v[8:11], v[136:139], v[234:237], v[8:11]
	v_mfma_f32_16x16x32_bf16 v[4:7], v[144:147], v[234:237], v[4:7]
	v_mfma_f32_16x16x32_bf16 v[64:67], v[148:151], v[190:193], 0
	v_mfma_f32_16x16x32_bf16 v[60:63], v[178:181], v[190:193], 0
	v_mfma_f32_16x16x32_bf16 v[48:51], v[148:151], v[198:201], 0
	v_mfma_f32_16x16x32_bf16 v[44:47], v[178:181], v[198:201], 0
	v_mfma_f32_16x16x32_bf16 v[32:35], v[148:151], v[222:225], 0
	v_mfma_f32_16x16x32_bf16 v[28:31], v[178:181], v[222:225], 0
	v_mfma_f32_16x16x32_bf16 v[16:19], v[148:151], v[230:233], 0
	v_mfma_f32_16x16x32_bf16 v[12:15], v[178:181], v[230:233], 0
	v_mfma_f32_16x16x32_bf16 v[64:67], v[152:155], v[194:197], v[64:67]
	v_mfma_f32_16x16x32_bf16 v[60:63], v[186:189], v[194:197], v[60:63]
	v_mfma_f32_16x16x32_bf16 v[48:51], v[152:155], v[202:205], v[48:51]
	v_mfma_f32_16x16x32_bf16 v[44:47], v[186:189], v[202:205], v[44:47]
	v_mfma_f32_16x16x32_bf16 v[32:35], v[152:155], v[226:229], v[32:35]
	v_mfma_f32_16x16x32_bf16 v[28:31], v[186:189], v[226:229], v[28:31]
	v_mfma_f32_16x16x32_bf16 v[16:19], v[152:155], v[234:237], v[16:19]
	v_mfma_f32_16x16x32_bf16 v[12:15], v[186:189], v[234:237], v[12:15]
	s_barrier
	s_setprio 0
	s_add_i32 s28, 0, 0x18000
	s_add_i32 s29, 0, 0x1c000
	v_add_u32_e32 v144, s28, v163
	v_add_u32_e32 v185, s29, v163
	ds_read_b128 v[132:135], v144
	ds_read_b128 v[136:139], v144 offset:1024
	ds_read_b128 v[140:143], v144 offset:2048
	ds_read_b128 v[144:147], v144 offset:3072
	ds_read_b128 v[148:151], v185
	ds_read_b128 v[152:155], v185 offset:1024
	ds_read_b128 v[178:181], v185 offset:2048
	ds_read_b128 v[186:189], v185 offset:3072
	s_add_u32 s100, s26, 0x80
	s_addc_u32 s101, s27, 0
	s_add_u32 s26, s26, 0x100000
	s_addc_u32 s27, s27, 0
	s_mov_b32 m0, s51
	ds_read_b128 v[190:193], v184 offset:32768
	ds_read_b128 v[194:197], v184 offset:33792
	ds_read_b128 v[198:201], v184 offset:34816
	ds_read_b128 v[202:205], v184 offset:35840
	ds_read_b128 v[222:225], v184 offset:36864
	ds_read_b128 v[226:229], v184 offset:37888
	ds_read_b128 v[230:233], v184 offset:38912
	ds_read_b128 v[234:237], v184 offset:39936
	global_load_lds_dwordx4 v172, s[26:27]
	s_mov_b32 m0, s54
	s_nop 0
	global_load_lds_dwordx4 v170, s[26:27]
	s_waitcnt vmcnt(8)
	s_waitcnt lgkmcnt(0)
	s_setprio 1
	s_barrier
	v_mfma_f32_16x16x32_bf16 v[120:123], v[132:135], v[190:193], v[120:123]
	v_mfma_f32_16x16x32_bf16 v[116:119], v[140:143], v[190:193], v[116:119]
	v_mfma_f32_16x16x32_bf16 v[104:107], v[132:135], v[198:201], v[104:107]
	v_mfma_f32_16x16x32_bf16 v[100:103], v[140:143], v[198:201], v[100:103]
	v_mfma_f32_16x16x32_bf16 v[88:91], v[132:135], v[222:225], v[88:91]
	v_mfma_f32_16x16x32_bf16 v[84:87], v[140:143], v[222:225], v[84:87]
	v_mfma_f32_16x16x32_bf16 v[72:75], v[132:135], v[230:233], v[72:75]
	v_mfma_f32_16x16x32_bf16 v[68:71], v[140:143], v[230:233], v[68:71]
	v_mfma_f32_16x16x32_bf16 v[120:123], v[136:139], v[194:197], v[120:123]
	v_mfma_f32_16x16x32_bf16 v[116:119], v[144:147], v[194:197], v[116:119]
	v_mfma_f32_16x16x32_bf16 v[104:107], v[136:139], v[202:205], v[104:107]
	v_mfma_f32_16x16x32_bf16 v[100:103], v[144:147], v[202:205], v[100:103]
	v_mfma_f32_16x16x32_bf16 v[88:91], v[136:139], v[226:229], v[88:91]
	v_mfma_f32_16x16x32_bf16 v[84:87], v[144:147], v[226:229], v[84:87]
	v_mfma_f32_16x16x32_bf16 v[72:75], v[136:139], v[234:237], v[72:75]
	v_mfma_f32_16x16x32_bf16 v[68:71], v[144:147], v[234:237], v[68:71]
	v_mfma_f32_16x16x32_bf16 v[128:131], v[148:151], v[190:193], v[128:131]
	v_mfma_f32_16x16x32_bf16 v[124:127], v[178:181], v[190:193], v[124:127]
	v_mfma_f32_16x16x32_bf16 v[112:115], v[148:151], v[198:201], v[112:115]
	v_mfma_f32_16x16x32_bf16 v[108:111], v[178:181], v[198:201], v[108:111]
	v_mfma_f32_16x16x32_bf16 v[96:99], v[148:151], v[222:225], v[96:99]
	v_mfma_f32_16x16x32_bf16 v[92:95], v[178:181], v[222:225], v[92:95]
	v_mfma_f32_16x16x32_bf16 v[80:83], v[148:151], v[230:233], v[80:83]
	v_mfma_f32_16x16x32_bf16 v[76:79], v[178:181], v[230:233], v[76:79]
	v_mfma_f32_16x16x32_bf16 v[128:131], v[152:155], v[194:197], v[128:131]
	v_mfma_f32_16x16x32_bf16 v[124:127], v[186:189], v[194:197], v[124:127]
	v_mfma_f32_16x16x32_bf16 v[112:115], v[152:155], v[202:205], v[112:115]
	v_mfma_f32_16x16x32_bf16 v[108:111], v[186:189], v[202:205], v[108:111]
	v_mfma_f32_16x16x32_bf16 v[96:99], v[152:155], v[226:229], v[96:99]
	v_mfma_f32_16x16x32_bf16 v[92:95], v[186:189], v[226:229], v[92:95]
	v_mfma_f32_16x16x32_bf16 v[80:83], v[152:155], v[234:237], v[80:83]
	v_mfma_f32_16x16x32_bf16 v[76:79], v[186:189], v[234:237], v[76:79]
	s_barrier
	s_setprio 0
	s_add_i32 s26, s28, s1
	s_add_u32 s24, s24, 0x80
	s_addc_u32 s25, s25, 0
	s_mov_b32 m0, s26
	ds_read_b128 v[190:193], v184 offset:49152
	ds_read_b128 v[194:197], v184 offset:50176
	ds_read_b128 v[198:201], v184 offset:51200
	ds_read_b128 v[202:205], v184 offset:52224
	ds_read_b128 v[222:225], v184 offset:53248
	ds_read_b128 v[226:229], v184 offset:54272
	ds_read_b128 v[230:233], v184 offset:55296
	ds_read_b128 v[234:237], v184 offset:56320
	global_load_lds_dwordx4 v2, s[24:25]
	s_add_i32 m0, s26, 0x2000
	s_add_i32 s26, s29, s1
	global_load_lds_dwordx4 v168, s[24:25]
	s_add_u32 s24, s24, 0x100000
	s_addc_u32 s25, s25, 0
	s_mov_b32 m0, s26
	s_nop 0
	global_load_lds_dwordx4 v2, s[24:25]
	s_add_i32 m0, s26, 0x2000
	s_nop 0
	global_load_lds_dwordx4 v168, s[24:25]
	s_mov_b32 m0, s78
	s_nop 0
	global_load_lds_dwordx4 v172, s[100:101]
	s_mov_b32 m0, s85
	s_nop 0
	global_load_lds_dwordx4 v170, s[100:101]
	s_waitcnt vmcnt(8)
	s_waitcnt lgkmcnt(0)
	s_setprio 1
	s_barrier
	v_mfma_f32_16x16x32_bf16 v[56:59], v[132:135], v[190:193], v[56:59]
	v_mfma_f32_16x16x32_bf16 v[52:55], v[140:143], v[190:193], v[52:55]
	v_mfma_f32_16x16x32_bf16 v[40:43], v[132:135], v[198:201], v[40:43]
	v_mfma_f32_16x16x32_bf16 v[36:39], v[140:143], v[198:201], v[36:39]
	v_mfma_f32_16x16x32_bf16 v[24:27], v[132:135], v[222:225], v[24:27]
	v_mfma_f32_16x16x32_bf16 v[20:23], v[140:143], v[222:225], v[20:23]
	v_mfma_f32_16x16x32_bf16 v[8:11], v[132:135], v[230:233], v[8:11]
	v_mfma_f32_16x16x32_bf16 v[4:7], v[140:143], v[230:233], v[4:7]
	v_mfma_f32_16x16x32_bf16 v[56:59], v[136:139], v[194:197], v[56:59]
	v_mfma_f32_16x16x32_bf16 v[52:55], v[144:147], v[194:197], v[52:55]
	v_mfma_f32_16x16x32_bf16 v[40:43], v[136:139], v[202:205], v[40:43]
	v_mfma_f32_16x16x32_bf16 v[36:39], v[144:147], v[202:205], v[36:39]
	v_mfma_f32_16x16x32_bf16 v[24:27], v[136:139], v[226:229], v[24:27]
	v_mfma_f32_16x16x32_bf16 v[20:23], v[144:147], v[226:229], v[20:23]
	v_mfma_f32_16x16x32_bf16 v[8:11], v[136:139], v[234:237], v[8:11]
	v_mfma_f32_16x16x32_bf16 v[4:7], v[144:147], v[234:237], v[4:7]
	v_mfma_f32_16x16x32_bf16 v[64:67], v[148:151], v[190:193], v[64:67]
	v_mfma_f32_16x16x32_bf16 v[60:63], v[178:181], v[190:193], v[60:63]
	v_mfma_f32_16x16x32_bf16 v[48:51], v[148:151], v[198:201], v[48:51]
	v_mfma_f32_16x16x32_bf16 v[44:47], v[178:181], v[198:201], v[44:47]
	v_mfma_f32_16x16x32_bf16 v[32:35], v[148:151], v[222:225], v[32:35]
	v_mfma_f32_16x16x32_bf16 v[28:31], v[178:181], v[222:225], v[28:31]
	v_mfma_f32_16x16x32_bf16 v[16:19], v[148:151], v[230:233], v[16:19]
	v_mfma_f32_16x16x32_bf16 v[12:15], v[178:181], v[230:233], v[12:15]
	v_mfma_f32_16x16x32_bf16 v[64:67], v[152:155], v[194:197], v[64:67]
	v_mfma_f32_16x16x32_bf16 v[60:63], v[186:189], v[194:197], v[60:63]
	v_mfma_f32_16x16x32_bf16 v[48:51], v[152:155], v[202:205], v[48:51]
	v_mfma_f32_16x16x32_bf16 v[44:47], v[186:189], v[202:205], v[44:47]
	v_mfma_f32_16x16x32_bf16 v[32:35], v[152:155], v[226:229], v[32:35]
	v_mfma_f32_16x16x32_bf16 v[28:31], v[186:189], v[226:229], v[28:31]
	v_mfma_f32_16x16x32_bf16 v[16:19], v[152:155], v[234:237], v[16:19]
	v_mfma_f32_16x16x32_bf16 v[12:15], v[186:189], v[234:237], v[12:15]
	s_barrier
	s_setprio 0
	s_add_i32 s58, s58, 2
	s_add_u32 s6, s6, 0x100
	s_addc_u32 s7, s7, 0
	s_add_u32 s21, s21, 0x100
	s_addc_u32 s13, s13, 0
	s_cmp_gt_u32 s58, 61
	s_cbranch_scc0 .LBB0_265
.LBB0_265:
	s_add_u32 s24, s6, 0xfff00080
	s_addc_u32 s25, s7, -1
	s_add_i32 s28, 0, 0x10000
	s_cmp_eq_u32 s58, 60
	s_cselect_b32 s27, s73, s25
	s_cselect_b32 s26, vcc_lo, s24
	s_cselect_b32 s25, s75, s13
	s_cselect_b32 s24, vcc_hi, s21
	s_add_i32 s71, 0, 0x14000
	v_add_u32_e32 v144, s28, v163
	v_add_u32_e32 v182, s71, v163
	s_waitcnt lgkmcnt(0)
	ds_read_b128 v[132:135], v144
	ds_read_b128 v[136:139], v144 offset:1024
	ds_read_b128 v[140:143], v144 offset:2048
	ds_read_b128 v[144:147], v144 offset:3072
	ds_read_b128 v[148:151], v182
	ds_read_b128 v[152:155], v182 offset:1024
	ds_read_b128 v[178:181], v182 offset:2048
	ds_read_b128 v[186:189], v182 offset:3072
	s_add_i32 m0, s46, 0xc000
	ds_read_b128 v[190:193], v184
	ds_read_b128 v[194:197], v184 offset:1024
	ds_read_b128 v[198:201], v184 offset:2048
	ds_read_b128 v[202:205], v184 offset:3072
	ds_read_b128 v[222:225], v184 offset:4096
	ds_read_b128 v[226:229], v184 offset:5120
	ds_read_b128 v[230:233], v184 offset:6144
	ds_read_b128 v[234:237], v184 offset:7168
	global_load_lds_dwordx4 v174, s[6:7]
	s_add_i32 m0, s46, 0xe000
	s_nop 0
	global_load_lds_dwordx4 v176, s[6:7]
	s_waitcnt vmcnt(8)
	s_waitcnt lgkmcnt(0)
	s_setprio 1
	s_barrier
	v_mfma_f32_16x16x32_bf16 v[120:123], v[132:135], v[190:193], v[120:123]
	v_mfma_f32_16x16x32_bf16 v[116:119], v[140:143], v[190:193], v[116:119]
	v_mfma_f32_16x16x32_bf16 v[104:107], v[132:135], v[198:201], v[104:107]
	v_mfma_f32_16x16x32_bf16 v[100:103], v[140:143], v[198:201], v[100:103]
	v_mfma_f32_16x16x32_bf16 v[88:91], v[132:135], v[222:225], v[88:91]
	v_mfma_f32_16x16x32_bf16 v[84:87], v[140:143], v[222:225], v[84:87]
	v_mfma_f32_16x16x32_bf16 v[72:75], v[132:135], v[230:233], v[72:75]
	v_mfma_f32_16x16x32_bf16 v[68:71], v[140:143], v[230:233], v[68:71]
	v_mfma_f32_16x16x32_bf16 v[120:123], v[136:139], v[194:197], v[120:123]
	v_mfma_f32_16x16x32_bf16 v[116:119], v[144:147], v[194:197], v[116:119]
	v_mfma_f32_16x16x32_bf16 v[104:107], v[136:139], v[202:205], v[104:107]
	v_mfma_f32_16x16x32_bf16 v[100:103], v[144:147], v[202:205], v[100:103]
	v_mfma_f32_16x16x32_bf16 v[88:91], v[136:139], v[226:229], v[88:91]
	v_mfma_f32_16x16x32_bf16 v[84:87], v[144:147], v[226:229], v[84:87]
	v_mfma_f32_16x16x32_bf16 v[72:75], v[136:139], v[234:237], v[72:75]
	v_mfma_f32_16x16x32_bf16 v[68:71], v[144:147], v[234:237], v[68:71]
	v_mfma_f32_16x16x32_bf16 v[128:131], v[148:151], v[190:193], v[128:131]
	v_mfma_f32_16x16x32_bf16 v[124:127], v[178:181], v[190:193], v[124:127]
	v_mfma_f32_16x16x32_bf16 v[112:115], v[148:151], v[198:201], v[112:115]
	v_mfma_f32_16x16x32_bf16 v[108:111], v[178:181], v[198:201], v[108:111]
	v_mfma_f32_16x16x32_bf16 v[96:99], v[148:151], v[222:225], v[96:99]
	v_mfma_f32_16x16x32_bf16 v[92:95], v[178:181], v[222:225], v[92:95]
	v_mfma_f32_16x16x32_bf16 v[80:83], v[148:151], v[230:233], v[80:83]
	v_mfma_f32_16x16x32_bf16 v[76:79], v[178:181], v[230:233], v[76:79]
	v_mfma_f32_16x16x32_bf16 v[128:131], v[152:155], v[194:197], v[128:131]
	v_mfma_f32_16x16x32_bf16 v[124:127], v[186:189], v[194:197], v[124:127]
	v_mfma_f32_16x16x32_bf16 v[112:115], v[152:155], v[202:205], v[112:115]
	v_mfma_f32_16x16x32_bf16 v[108:111], v[186:189], v[202:205], v[108:111]
	v_mfma_f32_16x16x32_bf16 v[96:99], v[152:155], v[226:229], v[96:99]
	v_mfma_f32_16x16x32_bf16 v[92:95], v[186:189], v[226:229], v[92:95]
	v_mfma_f32_16x16x32_bf16 v[80:83], v[152:155], v[234:237], v[80:83]
	v_mfma_f32_16x16x32_bf16 v[76:79], v[186:189], v[234:237], v[76:79]
	s_barrier
	s_setprio 0
	s_add_i32 s28, s28, s1
	s_mov_b32 m0, s28
	ds_read_b128 v[190:193], v184 offset:16384
	ds_read_b128 v[194:197], v184 offset:17408
	ds_read_b128 v[198:201], v184 offset:18432
	ds_read_b128 v[202:205], v184 offset:19456
	ds_read_b128 v[222:225], v184 offset:20480
	ds_read_b128 v[226:229], v184 offset:21504
	ds_read_b128 v[230:233], v184 offset:22528
	ds_read_b128 v[234:237], v184 offset:23552
	global_load_lds_dwordx4 v2, s[24:25]
	s_add_i32 m0, s28, 0x2000
	s_add_u32 s28, s24, 0x100000
	s_addc_u32 s29, s25, 0
	s_add_i32 s71, s71, s1
	global_load_lds_dwordx4 v168, s[24:25]
	s_mov_b32 m0, s71
	s_nop 0
	global_load_lds_dwordx4 v2, s[28:29]
	s_add_i32 m0, s71, 0x2000
	s_nop 0
	global_load_lds_dwordx4 v168, s[28:29]
	s_mov_b32 m0, s46
	s_nop 0
	global_load_lds_dwordx4 v172, s[26:27]
	s_mov_b32 m0, s50
	s_nop 0
	global_load_lds_dwordx4 v170, s[26:27]
	s_waitcnt vmcnt(8)
	s_waitcnt lgkmcnt(0)
	s_setprio 1
	s_barrier
	v_mfma_f32_16x16x32_bf16 v[56:59], v[132:135], v[190:193], v[56:59]
	v_mfma_f32_16x16x32_bf16 v[52:55], v[140:143], v[190:193], v[52:55]
	v_mfma_f32_16x16x32_bf16 v[40:43], v[132:135], v[198:201], v[40:43]
	v_mfma_f32_16x16x32_bf16 v[36:39], v[140:143], v[198:201], v[36:39]
	v_mfma_f32_16x16x32_bf16 v[24:27], v[132:135], v[222:225], v[24:27]
	v_mfma_f32_16x16x32_bf16 v[20:23], v[140:143], v[222:225], v[20:23]
	v_mfma_f32_16x16x32_bf16 v[8:11], v[132:135], v[230:233], v[8:11]
	v_mfma_f32_16x16x32_bf16 v[4:7], v[140:143], v[230:233], v[4:7]
	v_mfma_f32_16x16x32_bf16 v[56:59], v[136:139], v[194:197], v[56:59]
	v_mfma_f32_16x16x32_bf16 v[52:55], v[144:147], v[194:197], v[52:55]
	v_mfma_f32_16x16x32_bf16 v[40:43], v[136:139], v[202:205], v[40:43]
	v_mfma_f32_16x16x32_bf16 v[36:39], v[144:147], v[202:205], v[36:39]
	v_mfma_f32_16x16x32_bf16 v[24:27], v[136:139], v[226:229], v[24:27]
	v_mfma_f32_16x16x32_bf16 v[20:23], v[144:147], v[226:229], v[20:23]
	v_mfma_f32_16x16x32_bf16 v[8:11], v[136:139], v[234:237], v[8:11]
	v_mfma_f32_16x16x32_bf16 v[4:7], v[144:147], v[234:237], v[4:7]
	v_mfma_f32_16x16x32_bf16 v[64:67], v[148:151], v[190:193], v[64:67]
	v_mfma_f32_16x16x32_bf16 v[60:63], v[178:181], v[190:193], v[60:63]
	v_mfma_f32_16x16x32_bf16 v[48:51], v[148:151], v[198:201], v[48:51]
	v_mfma_f32_16x16x32_bf16 v[44:47], v[178:181], v[198:201], v[44:47]
	v_mfma_f32_16x16x32_bf16 v[32:35], v[148:151], v[222:225], v[32:35]
	v_mfma_f32_16x16x32_bf16 v[28:31], v[178:181], v[222:225], v[28:31]
	v_mfma_f32_16x16x32_bf16 v[16:19], v[148:151], v[230:233], v[16:19]
	v_mfma_f32_16x16x32_bf16 v[12:15], v[178:181], v[230:233], v[12:15]
	v_mfma_f32_16x16x32_bf16 v[64:67], v[152:155], v[194:197], v[64:67]
	v_mfma_f32_16x16x32_bf16 v[60:63], v[186:189], v[194:197], v[60:63]
	v_mfma_f32_16x16x32_bf16 v[48:51], v[152:155], v[202:205], v[48:51]
	v_mfma_f32_16x16x32_bf16 v[44:47], v[186:189], v[202:205], v[44:47]
	v_mfma_f32_16x16x32_bf16 v[32:35], v[152:155], v[226:229], v[32:35]
	v_mfma_f32_16x16x32_bf16 v[28:31], v[186:189], v[226:229], v[28:31]
	v_mfma_f32_16x16x32_bf16 v[16:19], v[152:155], v[234:237], v[16:19]
	v_mfma_f32_16x16x32_bf16 v[12:15], v[186:189], v[234:237], v[12:15]
	s_barrier
	s_setprio 0
	s_add_i32 s28, 0, 0x18000
	s_add_i32 s29, 0, 0x1c000
	v_add_u32_e32 v144, s28, v163
	v_add_u32_e32 v185, s29, v163
	ds_read_b128 v[132:135], v144
	ds_read_b128 v[136:139], v144 offset:1024
	ds_read_b128 v[140:143], v144 offset:2048
	ds_read_b128 v[144:147], v144 offset:3072
	ds_read_b128 v[148:151], v185
	ds_read_b128 v[152:155], v185 offset:1024
	ds_read_b128 v[178:181], v185 offset:2048
	ds_read_b128 v[186:189], v185 offset:3072
	s_add_u32 s100, s26, 0x80
	s_addc_u32 s101, s27, 0
	s_add_u32 s26, s26, 0x100000
	s_addc_u32 s27, s27, 0
	s_mov_b32 m0, s51
	ds_read_b128 v[190:193], v184 offset:32768
	ds_read_b128 v[194:197], v184 offset:33792
	ds_read_b128 v[198:201], v184 offset:34816
	ds_read_b128 v[202:205], v184 offset:35840
	ds_read_b128 v[222:225], v184 offset:36864
	ds_read_b128 v[226:229], v184 offset:37888
	ds_read_b128 v[230:233], v184 offset:38912
	ds_read_b128 v[234:237], v184 offset:39936
	global_load_lds_dwordx4 v172, s[26:27]
	s_mov_b32 m0, s54
	s_nop 0
	global_load_lds_dwordx4 v170, s[26:27]
	s_waitcnt vmcnt(8)
	s_waitcnt lgkmcnt(0)
	s_setprio 1
	s_barrier
	v_mfma_f32_16x16x32_bf16 v[120:123], v[132:135], v[190:193], v[120:123]
	v_mfma_f32_16x16x32_bf16 v[116:119], v[140:143], v[190:193], v[116:119]
	v_mfma_f32_16x16x32_bf16 v[104:107], v[132:135], v[198:201], v[104:107]
	v_mfma_f32_16x16x32_bf16 v[100:103], v[140:143], v[198:201], v[100:103]
	v_mfma_f32_16x16x32_bf16 v[88:91], v[132:135], v[222:225], v[88:91]
	v_mfma_f32_16x16x32_bf16 v[84:87], v[140:143], v[222:225], v[84:87]
	v_mfma_f32_16x16x32_bf16 v[72:75], v[132:135], v[230:233], v[72:75]
	v_mfma_f32_16x16x32_bf16 v[68:71], v[140:143], v[230:233], v[68:71]
	v_mfma_f32_16x16x32_bf16 v[120:123], v[136:139], v[194:197], v[120:123]
	v_mfma_f32_16x16x32_bf16 v[116:119], v[144:147], v[194:197], v[116:119]
	v_mfma_f32_16x16x32_bf16 v[104:107], v[136:139], v[202:205], v[104:107]
	v_mfma_f32_16x16x32_bf16 v[100:103], v[144:147], v[202:205], v[100:103]
	v_mfma_f32_16x16x32_bf16 v[88:91], v[136:139], v[226:229], v[88:91]
	v_mfma_f32_16x16x32_bf16 v[84:87], v[144:147], v[226:229], v[84:87]
	v_mfma_f32_16x16x32_bf16 v[72:75], v[136:139], v[234:237], v[72:75]
	v_mfma_f32_16x16x32_bf16 v[68:71], v[144:147], v[234:237], v[68:71]
	v_mfma_f32_16x16x32_bf16 v[128:131], v[148:151], v[190:193], v[128:131]
	v_mfma_f32_16x16x32_bf16 v[124:127], v[178:181], v[190:193], v[124:127]
	v_mfma_f32_16x16x32_bf16 v[112:115], v[148:151], v[198:201], v[112:115]
	v_mfma_f32_16x16x32_bf16 v[108:111], v[178:181], v[198:201], v[108:111]
	v_mfma_f32_16x16x32_bf16 v[96:99], v[148:151], v[222:225], v[96:99]
	v_mfma_f32_16x16x32_bf16 v[92:95], v[178:181], v[222:225], v[92:95]
	v_mfma_f32_16x16x32_bf16 v[80:83], v[148:151], v[230:233], v[80:83]
	v_mfma_f32_16x16x32_bf16 v[76:79], v[178:181], v[230:233], v[76:79]
	v_mfma_f32_16x16x32_bf16 v[128:131], v[152:155], v[194:197], v[128:131]
	v_mfma_f32_16x16x32_bf16 v[124:127], v[186:189], v[194:197], v[124:127]
	v_mfma_f32_16x16x32_bf16 v[112:115], v[152:155], v[202:205], v[112:115]
	v_mfma_f32_16x16x32_bf16 v[108:111], v[186:189], v[202:205], v[108:111]
	v_mfma_f32_16x16x32_bf16 v[96:99], v[152:155], v[226:229], v[96:99]
	v_mfma_f32_16x16x32_bf16 v[92:95], v[186:189], v[226:229], v[92:95]
	v_mfma_f32_16x16x32_bf16 v[80:83], v[152:155], v[234:237], v[80:83]
	v_mfma_f32_16x16x32_bf16 v[76:79], v[186:189], v[234:237], v[76:79]
	s_barrier
	s_setprio 0
	s_add_i32 s26, s28, s1
	s_add_u32 s24, s24, 0x80
	s_addc_u32 s25, s25, 0
	s_mov_b32 m0, s26
	ds_read_b128 v[190:193], v184 offset:49152
	ds_read_b128 v[194:197], v184 offset:50176
	ds_read_b128 v[198:201], v184 offset:51200
	ds_read_b128 v[202:205], v184 offset:52224
	ds_read_b128 v[222:225], v184 offset:53248
	ds_read_b128 v[226:229], v184 offset:54272
	ds_read_b128 v[230:233], v184 offset:55296
	ds_read_b128 v[234:237], v184 offset:56320
	global_load_lds_dwordx4 v2, s[24:25]
	s_add_i32 m0, s26, 0x2000
	s_add_i32 s26, s29, s1
	global_load_lds_dwordx4 v168, s[24:25]
	s_add_u32 s24, s24, 0x100000
	s_addc_u32 s25, s25, 0
	s_mov_b32 m0, s26
	s_nop 0
	global_load_lds_dwordx4 v2, s[24:25]
	s_add_i32 m0, s26, 0x2000
	s_nop 0
	global_load_lds_dwordx4 v168, s[24:25]
	s_mov_b32 m0, s78
	s_nop 0
	global_load_lds_dwordx4 v172, s[100:101]
	s_mov_b32 m0, s85
	s_nop 0
	global_load_lds_dwordx4 v170, s[100:101]
	s_waitcnt vmcnt(8)
	s_waitcnt lgkmcnt(0)
	s_setprio 1
	s_barrier
	v_mfma_f32_16x16x32_bf16 v[56:59], v[132:135], v[190:193], v[56:59]
	v_mfma_f32_16x16x32_bf16 v[52:55], v[140:143], v[190:193], v[52:55]
	v_mfma_f32_16x16x32_bf16 v[40:43], v[132:135], v[198:201], v[40:43]
	v_mfma_f32_16x16x32_bf16 v[36:39], v[140:143], v[198:201], v[36:39]
	v_mfma_f32_16x16x32_bf16 v[24:27], v[132:135], v[222:225], v[24:27]
	v_mfma_f32_16x16x32_bf16 v[20:23], v[140:143], v[222:225], v[20:23]
	v_mfma_f32_16x16x32_bf16 v[8:11], v[132:135], v[230:233], v[8:11]
	v_mfma_f32_16x16x32_bf16 v[4:7], v[140:143], v[230:233], v[4:7]
	v_mfma_f32_16x16x32_bf16 v[56:59], v[136:139], v[194:197], v[56:59]
	v_mfma_f32_16x16x32_bf16 v[52:55], v[144:147], v[194:197], v[52:55]
	v_mfma_f32_16x16x32_bf16 v[40:43], v[136:139], v[202:205], v[40:43]
	v_mfma_f32_16x16x32_bf16 v[36:39], v[144:147], v[202:205], v[36:39]
	v_mfma_f32_16x16x32_bf16 v[24:27], v[136:139], v[226:229], v[24:27]
	v_mfma_f32_16x16x32_bf16 v[20:23], v[144:147], v[226:229], v[20:23]
	v_mfma_f32_16x16x32_bf16 v[8:11], v[136:139], v[234:237], v[8:11]
	v_mfma_f32_16x16x32_bf16 v[4:7], v[144:147], v[234:237], v[4:7]
	v_mfma_f32_16x16x32_bf16 v[64:67], v[148:151], v[190:193], v[64:67]
	v_mfma_f32_16x16x32_bf16 v[60:63], v[178:181], v[190:193], v[60:63]
	v_mfma_f32_16x16x32_bf16 v[48:51], v[148:151], v[198:201], v[48:51]
	v_mfma_f32_16x16x32_bf16 v[44:47], v[178:181], v[198:201], v[44:47]
	v_mfma_f32_16x16x32_bf16 v[32:35], v[148:151], v[222:225], v[32:35]
	v_mfma_f32_16x16x32_bf16 v[28:31], v[178:181], v[222:225], v[28:31]
	v_mfma_f32_16x16x32_bf16 v[16:19], v[148:151], v[230:233], v[16:19]
	v_mfma_f32_16x16x32_bf16 v[12:15], v[178:181], v[230:233], v[12:15]
	v_mfma_f32_16x16x32_bf16 v[64:67], v[152:155], v[194:197], v[64:67]
	v_mfma_f32_16x16x32_bf16 v[60:63], v[186:189], v[194:197], v[60:63]
	v_mfma_f32_16x16x32_bf16 v[48:51], v[152:155], v[202:205], v[48:51]
	v_mfma_f32_16x16x32_bf16 v[44:47], v[186:189], v[202:205], v[44:47]
	v_mfma_f32_16x16x32_bf16 v[32:35], v[152:155], v[226:229], v[32:35]
	v_mfma_f32_16x16x32_bf16 v[28:31], v[186:189], v[226:229], v[28:31]
	v_mfma_f32_16x16x32_bf16 v[16:19], v[152:155], v[234:237], v[16:19]
	v_mfma_f32_16x16x32_bf16 v[12:15], v[186:189], v[234:237], v[12:15]
	s_barrier
	s_setprio 0
	s_add_i32 s58, s58, 2
	s_add_u32 s6, s6, 0x100
	s_addc_u32 s7, s7, 0
	s_add_u32 s21, s21, 0x100
	s_addc_u32 s13, s13, 0
	s_cmp_gt_u32 s58, 61
	s_cbranch_scc0 .LBB0_265
	s_and_b64 vcc, exec, s[30:31]
	s_cbranch_vccz .LBB0_268
	s_barrier
